# converter queue pull: stop flag read one item stale (one pipeline drain fewer per item), on top of 64 converters + walk wait fix
# speedup vs baseline: 1.0301x; 1.0084x over previous
; #define GAS __attribute__((address_space(1)))
; #define P0_GET() do { if (DYN) { int v_ = 0x7fffffff; if (lane == 0) { if (!check_stop || __hip_atomic_load(stopw, RLX_AGENT) == 0u) v_ = (int)atomicAdd(qword, 1u); } \
;         idx = __builtin_amdgcn_readfirstlane(v_); ok = idx < P0_NHALF; } else { idx = cur_static; cur_static += nw; ok = idx < s1; } } while (0)
; #define P0_MAKE() (DYN ? p0_strip_half(args, ws, idx) : p0_strip(args, ws, idx))
; #define P0_LD(B_) do { if (lv) { p0_load(B_, lst, lj, lane); if (++lj == lst.nk) { lj = 0; P0_GET(); if (ok) { lst = P0_MAKE(); nst = lst; has_n = true; } else lv = false; } } } while (0)
; __device__ __forceinline__ void p0_load(f32x4 (&v)[8], const Strip& st, int j, int lane) {
;     const float* p = st.src + (size_t)(j * 64 + (lane >> 3)) * st.ldw + (lane & 7) * 4;
; #pragma unroll
;     for (int i = 0; i < 8; ++i) v[i] = __builtin_nontemporal_load((const GAS f32x4*)(p + (size_t)(i * 8) * st.ldw));
; }
; template <bool DYN>
; __device__ __forceinline__ void p0_walk(const Args& args, unsigned char* ws, LAS float* scr, int lane, int w, int nw, int s0, int s1, unsigned* qword, unsigned* stopw, bool check_stop) {
;     ...
;     P0_GET();
;     if (!ok) return;
;     Strip lst = P0_MAKE(), sst = lst, nst = lst; bool has_n = false, lv = true, sv = true; int lj = 0, sj = 0;
;     f32x4 b0[8], b1[8], b2[8], b3[8]; u32x2 hold[4];
;     ...
;     P0_LD(b0); P0_LD(b1); P0_LD(b2);
.LBB0_33:
	s_lshl_b32 s17, s17, 5
	s_lshl_b32 s22, s74, 14
	s_and_b32 s17, s17, 0x7e0
	s_add_i32 s22, s22, 0
	s_lshl_b32 s23, s17, 2
	s_add_u32 s23, s38, s23
	s_addc_u32 s26, s39, 0
	s_lshl_b32 s3, s3, 9
	s_and_b32 s3, s3, 0x600
	s_lshl_b32 s27, s3, 13
	s_add_u32 s44, s23, s27
	v_lshrrev_b32_e32 v133, 3, v164
	s_addc_u32 s45, s26, 0
	v_lshlrev_b32_e32 v130, 13, v133
	v_mov_b32_e32 v131, 0
	v_and_b32_e32 v132, 28, v166
	v_lshl_add_u64 v[2:3], s[44:45], 0, v[130:131]
	v_lshlrev_b32_e32 v130, 2, v132
	v_lshl_add_u64 v[74:75], v[2:3], 0, v[130:131]
	s_mov_b32 s23, 0x10000
	v_add_co_u32_e32 v6, vcc, s23, v74
	s_mov_b32 s23, 0x20000
	s_nop 0
	v_addc_co_u32_e32 v7, vcc, 0, v75, vcc
	v_add_co_u32_e32 v10, vcc, s23, v74
	s_mov_b32 s23, 0x30000
	s_nop 0
	v_addc_co_u32_e32 v11, vcc, 0, v75, vcc
	v_add_co_u32_e32 v14, vcc, s23, v74
	s_mov_b32 s23, 0x40000
	s_nop 0
	v_addc_co_u32_e32 v15, vcc, 0, v75, vcc
	v_add_co_u32_e32 v18, vcc, s23, v74
	s_mov_b32 s23, 0x50000
	s_nop 0
	v_addc_co_u32_e32 v19, vcc, 0, v75, vcc
	v_add_co_u32_e32 v22, vcc, s23, v74
	s_mov_b32 s23, 0x60000
	s_nop 0
	v_addc_co_u32_e32 v23, vcc, 0, v75, vcc
	v_add_co_u32_e32 v26, vcc, s23, v74
	s_mov_b32 s23, 0x70000
	s_nop 0
	v_addc_co_u32_e32 v27, vcc, 0, v75, vcc
	v_add_co_u32_e32 v30, vcc, s23, v74
	s_mov_b32 s23, 0x80000
	s_nop 0
	v_addc_co_u32_e32 v31, vcc, 0, v75, vcc
	v_add_co_u32_e32 v34, vcc, s23, v74
	s_mov_b32 s23, 0x90000
	s_nop 0
	v_addc_co_u32_e32 v35, vcc, 0, v75, vcc
	v_add_co_u32_e32 v38, vcc, s23, v74
	s_mov_b32 s23, 0xa0000
	s_nop 0
	v_addc_co_u32_e32 v39, vcc, 0, v75, vcc
	v_add_co_u32_e32 v42, vcc, s23, v74
	s_mov_b32 s23, 0xb0000
	s_nop 0
	v_addc_co_u32_e32 v43, vcc, 0, v75, vcc
	v_add_co_u32_e32 v46, vcc, s23, v74
	s_mov_b32 s23, 0xc0000
	s_nop 0
	v_addc_co_u32_e32 v47, vcc, 0, v75, vcc
	v_add_co_u32_e32 v50, vcc, s23, v74
	s_mov_b32 s23, 0xd0000
	s_nop 0
	v_addc_co_u32_e32 v51, vcc, 0, v75, vcc
	v_add_co_u32_e32 v54, vcc, s23, v74
	s_mov_b32 s23, 0xe0000
	s_nop 0
	v_addc_co_u32_e32 v55, vcc, 0, v75, vcc
	v_add_co_u32_e32 v58, vcc, s23, v74
	s_mov_b32 s23, 0xf0000
	s_nop 0
	v_addc_co_u32_e32 v59, vcc, 0, v75, vcc
	v_add_co_u32_e32 v62, vcc, s23, v74
	s_mov_b32 s23, 0x100000
	s_nop 0
	v_addc_co_u32_e32 v63, vcc, 0, v75, vcc
	v_add_co_u32_e32 v66, vcc, s23, v74
	s_mov_b32 s23, 0x110000
	s_nop 0
	v_addc_co_u32_e32 v67, vcc, 0, v75, vcc
	v_add_co_u32_e32 v70, vcc, s23, v74
	s_mov_b32 s23, 0x120000
	s_nop 0
	v_addc_co_u32_e32 v71, vcc, 0, v75, vcc
	v_add_co_u32_e32 v76, vcc, s23, v74
	s_mov_b32 s23, 0x130000
	s_nop 0
	v_addc_co_u32_e32 v77, vcc, 0, v75, vcc
	v_add_co_u32_e32 v78, vcc, s23, v74
	s_mov_b32 s23, 0x140000
	s_nop 0
	v_addc_co_u32_e32 v79, vcc, 0, v75, vcc
	global_load_dwordx4 v[2:5], v[74:75], off nt
	s_nop 0
	global_load_dwordx4 v[6:9], v[6:7], off nt
	s_nop 0
	global_load_dwordx4 v[10:13], v[10:11], off nt
	s_nop 0
	global_load_dwordx4 v[14:17], v[14:15], off nt
	s_nop 0
	global_load_dwordx4 v[18:21], v[18:19], off nt
	s_nop 0
	global_load_dwordx4 v[22:25], v[22:23], off nt
	s_nop 0
	global_load_dwordx4 v[26:29], v[26:27], off nt
	s_nop 0
	global_load_dwordx4 v[30:33], v[30:31], off nt
	s_nop 0
	global_load_dwordx4 v[34:37], v[34:35], off nt
	s_nop 0
	global_load_dwordx4 v[38:41], v[38:39], off nt
	s_nop 0
	global_load_dwordx4 v[42:45], v[42:43], off nt
	s_nop 0
	global_load_dwordx4 v[46:49], v[46:47], off nt
	s_nop 0
	global_load_dwordx4 v[50:53], v[50:51], off nt
	s_nop 0
	global_load_dwordx4 v[54:57], v[54:55], off nt
	s_nop 0
	global_load_dwordx4 v[58:61], v[58:59], off nt
	s_nop 0
	global_load_dwordx4 v[62:65], v[62:63], off nt
	s_nop 0
	global_load_dwordx4 v[66:69], v[66:67], off nt
	s_nop 0
	global_load_dwordx4 v[70:73], v[70:71], off nt
	s_nop 0
	global_load_dwordx4 v[82:85], v[76:77], off nt
	global_load_dwordx4 v[86:89], v[78:79], off nt
	v_add_co_u32_e32 v76, vcc, s23, v74
	s_mov_b32 s23, 0x150000
	s_nop 0
	v_addc_co_u32_e32 v77, vcc, 0, v75, vcc
	v_add_co_u32_e32 v78, vcc, s23, v74
	s_mov_b32 s23, 0x160000
	s_nop 0
	v_addc_co_u32_e32 v79, vcc, 0, v75, vcc
	global_load_dwordx4 v[98:101], v[76:77], off nt
	global_load_dwordx4 v[102:105], v[78:79], off nt
	v_add_co_u32_e32 v76, vcc, s23, v74
	s_mov_b32 s23, 0x170000
	s_nop 0
	v_addc_co_u32_e32 v77, vcc, 0, v75, vcc
	v_add_co_u32_e32 v74, vcc, s23, v74
	s_add_u32 s42, s10, s3
	s_nop 0
	v_addc_co_u32_e32 v75, vcc, 0, v75, vcc
	global_load_dwordx4 v[114:117], v[76:77], off nt
	global_load_dwordx4 v[122:125], v[74:75], off nt
	s_addc_u32 s43, s11, 0
	s_load_dwordx2 s[10:11], s[0:1], 0x78
	s_load_dwordx2 s[38:39], s[0:1], 0x88
	s_load_dwordx2 s[40:41], s[0:1], 0x98
	v_and_b32_e32 v76, 7, v0
	v_add_u32_e32 v74, s22, v130
	v_mul_u32_u24_e32 v75, 0x84, v133
	v_lshlrev_b32_e32 v134, 3, v76
	v_mul_u32_u24_e32 v76, 0x420, v76
	v_lshlrev_b32_e32 v77, 2, v133
	s_mov_b32 s26, 0
	s_mov_b32 s3, 3
	v_or_b32_e32 v165, 8, v133
	v_or_b32_e32 v167, 16, v133
	v_or_b32_e32 v182, 24, v133
	v_mov_b32_e32 v135, v131
	v_add3_u32 v183, s22, v76, v77
	s_mov_b64 s[48:49], -1
	s_mov_b64 s[52:53], 0
	s_movk_i32 s60, 0x2000
	s_mov_b32 s61, 0x7fffff00
	s_movk_i32 s62, 0x7f
	s_movk_i32 s63, 0x80
	s_mov_b32 s64, 0xaaaaaaab
	s_movk_i32 s65, 0xc0
	s_movk_i32 s66, 0x3ff
	s_movk_i32 s67, 0x440
	v_add_u32_e32 v184, v74, v75
	s_mov_b64 s[46:47], s[42:43]
	s_mov_b32 s68, s16
	s_mov_b32 s69, s17
	v_mov_b32_e32 v255, 0
	s_branch .LBB0_35

; #define P0_GET() do { if (DYN) { int v_ = 0x7fffffff; if (lane == 0) { if (!check_stop || __hip_atomic_load(stopw, RLX_AGENT) == 0u) v_ = (int)atomicAdd(qword, 1u); } \
;         idx = __builtin_amdgcn_readfirstlane(v_); ok = idx < P0_NHALF; } else { idx = cur_static; cur_static += nw; ok = idx < s1; } } while (0)
; #define P0_MAKE() (DYN ? p0_strip_half(args, ws, idx) : p0_strip(args, ws, idx))
; template <bool DYN>
; __device__ __forceinline__ void p0_walk(const Args& args, unsigned char* ws, LAS float* scr, int lane, int w, int nw, int s0, int s1, unsigned* qword, unsigned* stopw, bool check_stop) {
;     ...
;     P0_GET();
;     if (!ok) return;
;     Strip lst = P0_MAKE(), sst = lst, nst = lst; bool has_n = false, lv = true, sv = true; int lj = 0, sj = 0;
;     f32x4 b0[8], b1[8], b2[8], b3[8]; u32x2 hold[4];
.LBB0_35:
	s_andn2_b64 vcc, exec, s[48:49]
	s_cbranch_vccnz .LBB0_53
	v_lshl_or_b32 v130, s3, 6, v133
	v_lshlrev_b64 v[74:75], 13, v[130:131]
	v_lshl_add_u64 v[74:75], s[44:45], 0, v[74:75]
	v_lshlrev_b32_e32 v130, 2, v132
	v_lshl_add_u64 v[118:119], v[74:75], 0, v[130:131]
	v_add_co_u32_e32 v78, vcc, 0x10000, v118
	s_add_i32 s3, s3, 1
	s_nop 0
	v_addc_co_u32_e32 v79, vcc, 0, v119, vcc
	v_add_co_u32_e32 v90, vcc, 0x20000, v118
	global_load_dwordx4 v[74:77], v[118:119], off nt
	s_nop 0
	global_load_dwordx4 v[78:81], v[78:79], off nt
	v_addc_co_u32_e32 v91, vcc, 0, v119, vcc
	v_add_co_u32_e32 v94, vcc, 0x30000, v118
	s_cmp_lg_u32 s3, 8
	s_nop 0
	v_addc_co_u32_e32 v95, vcc, 0, v119, vcc
	v_add_co_u32_e32 v106, vcc, 0x40000, v118
	global_load_dwordx4 v[90:93], v[90:91], off nt
	s_nop 0
	global_load_dwordx4 v[94:97], v[94:95], off nt
	v_addc_co_u32_e32 v107, vcc, 0, v119, vcc
	v_add_co_u32_e32 v110, vcc, 0x50000, v118
	s_mov_b64 s[48:49], -1
	s_nop 0
	v_addc_co_u32_e32 v111, vcc, 0, v119, vcc
	v_add_co_u32_e32 v120, vcc, 0x60000, v118
	global_load_dwordx4 v[106:109], v[106:107], off nt
	s_nop 0
	global_load_dwordx4 v[110:113], v[110:111], off nt
	v_addc_co_u32_e32 v121, vcc, 0, v119, vcc
	v_add_co_u32_e32 v126, vcc, 0x70000, v118
	s_nop 1
	v_addc_co_u32_e32 v127, vcc, 0, v119, vcc
	global_load_dwordx4 v[118:121], v[120:121], off nt
	s_nop 0
	global_load_dwordx4 v[126:129], v[126:127], off nt
	s_cbranch_scc1 .LBB0_54
	v_bfrev_b32_e32 v130, -2
	s_and_saveexec_b64 s[48:49], s[4:5]
	s_cbranch_execz .LBB0_42
	v_mov_b32_e32 v130, v255
	global_load_dword v255, v131, s[6:7] sc1
	v_cmp_ne_u32_e32 vcc, 0, v130
	v_bfrev_b32_e32 v130, -2
	s_cbranch_vccnz .LBB0_42
	s_mov_b64 s[54:55], exec
	v_mbcnt_lo_u32_b32 v130, s54, 0
	v_mbcnt_hi_u32_b32 v130, s55, v130
	v_cmp_eq_u32_e32 vcc, 0, v130
	s_and_saveexec_b64 s[50:51], vcc
	s_cbranch_execz .LBB0_41
	s_bcnt1_i32_b64 s3, s[54:55]
	s_waitcnt lgkmcnt(0)
	v_mov_b32_e32 v136, s3
	global_atomic_add v136, v131, v136, s[8:9] sc0
